# v16 + MoE scatter phase: serial LDS integer sums issue their reads in batches (column sums 16 in flight per trip, prefix loops 8 per trip)
# baseline (speedup 1.0000x reference)
.LBB0_1408:
	v_lshl_add_u32 v8, s1, 6, v3
	v_lshl_add_u32 v9, s0, 6, v3
	ds_read2_b32 v[54:55], v8 offset1:32
	ds_read2_b32 v[56:57], v9 offset1:32
	ds_read2_b32 v[58:59], v8 offset0:64 offset1:96
	ds_read2_b32 v[60:61], v9 offset0:64 offset1:96
	ds_read2_b32 v[62:63], v8 offset0:128 offset1:160
	ds_read2_b32 v[64:65], v9 offset0:128 offset1:160
	ds_read2_b32 v[66:67], v8 offset0:192 offset1:224
	ds_read2_b32 v[68:69], v9 offset0:192 offset1:224
	s_add_i32 s1, s1, 16
	s_add_i32 s0, s0, 16
	s_add_i32 s4, s4, -16
	s_cmp_eq_u32 s4, 0
	s_waitcnt lgkmcnt(0)
	v_add3_u32 v2, v54, v2, v55
	v_add3_u32 v1, v56, v1, v57
	v_add3_u32 v2, v58, v2, v59
	v_add3_u32 v1, v60, v1, v61
	v_add3_u32 v2, v62, v2, v63
	v_add3_u32 v1, v64, v1, v65
	v_add3_u32 v2, v66, v2, v67
	v_add3_u32 v1, v68, v1, v69
	s_cbranch_scc0 .LBB0_1408
	v_add_u32_e32 v1, v2, v1
	v_add_u32_e32 v2, 0x140c0, v3
	ds_write_b32 v2, v1

.LBB0_1412:
	s_lshl_b32 s6, s1, 8
	v_add_u32_e32 v54, s6, v3
	ds_read_b32 v56, v54 offset:16128
	ds_read_b32 v57, v54 offset:16384
	ds_read_b32 v58, v54 offset:16640
	ds_read_b32 v59, v54 offset:16896
	ds_read_b32 v60, v54 offset:17152
	ds_read_b32 v61, v54 offset:17408
	ds_read_b32 v62, v54 offset:17664
	ds_read_b32 v63, v54 offset:17920
	ds_read_b32 v64, v54 offset:18176
	ds_read_b32 v65, v54 offset:18432
	ds_read_b32 v66, v54 offset:18688
	ds_read_b32 v67, v54 offset:18944
	ds_read_b32 v68, v54 offset:19200
	ds_read_b32 v69, v54 offset:19456
	ds_read_b32 v70, v54 offset:19712
	ds_read_b32 v71, v54 offset:19968
	s_add_i32 s1, s1, 16
	s_add_i32 s0, s0, 16
	s_add_i32 s4, s4, -16
	s_cmp_lg_u32 s4, 0
	s_waitcnt lgkmcnt(0)
	v_add3_u32 v2, v56, v2, v58
	v_add3_u32 v1, v57, v1, v59
	v_add3_u32 v2, v60, v2, v62
	v_add3_u32 v1, v61, v1, v63
	v_add3_u32 v2, v64, v2, v66
	v_add3_u32 v1, v65, v1, v67
	v_add3_u32 v2, v68, v2, v70
	v_add3_u32 v1, v69, v1, v71
	s_cbranch_scc1 .LBB0_1412
	v_add_u32_e32 v1, v2, v1
	v_add_u32_e32 v2, 0x14000, v3
	ds_write_b32 v2, v1
	v_add_u32_e32 v1, 0x14100, v3
	ds_write_b32 v1, v203

.Lsc_p8a:
	s_cmp_lt_u32 s39, 8
	s_cbranch_scc1 .Lsc_p2a
	v_lshl_add_u32 v54, s38, 8, v23
	ds_read_b32 v56, v54 offset:16384
	ds_read_b32 v57, v54 offset:16640
	ds_read_b32 v58, v54 offset:16896
	ds_read_b32 v59, v54 offset:17152
	ds_read_b32 v60, v54 offset:17408
	ds_read_b32 v61, v54 offset:17664
	ds_read_b32 v62, v54 offset:17920
	ds_read_b32 v63, v54 offset:18176
	s_add_i32 s38, s38, 8
	s_add_i32 s1, s1, 8
	s_add_i32 s39, s39, -8
	s_waitcnt lgkmcnt(0)
	v_add3_u32 v4, v56, v4, v58
	v_add3_u32 v5, v57, v5, v59
	v_add3_u32 v4, v60, v4, v62
	v_add3_u32 v5, v61, v5, v63
	s_branch .Lsc_p8a
.Lsc_p2a:
	s_cmp_eq_u32 s39, 0
	s_cbranch_scc1 .Lsc_pda

.Lsc_pda:
	s_and_b32 s1, s70, 0x7ffffffe
	s_cmp_lg_u32 s70, s1
	v_add_u32_e32 v4, v4, v5
	s_cselect_b64 s[38:39], -1, 0
	s_and_b64 vcc, exec, s[38:39]
	s_cbranch_vccnz .LBB0_1557
	s_branch .LBB0_1559

.Lsc_p8b:
	s_cmp_lt_u32 s0, 8
	s_cbranch_scc1 .Lsc_p2b
	v_lshl_add_u32 v54, s38, 6, v23
	ds_read_b32 v56, v54 offset:0
	ds_read_b32 v57, v54 offset:64
	ds_read_b32 v58, v54 offset:128
	ds_read_b32 v59, v54 offset:192
	ds_read_b32 v60, v54 offset:256
	ds_read_b32 v61, v54 offset:320
	ds_read_b32 v62, v54 offset:384
	ds_read_b32 v63, v54 offset:448
	s_add_i32 s38, s38, 8
	s_add_i32 s1, s1, 8
	s_add_i32 s0, s0, -8
	s_waitcnt lgkmcnt(0)
	v_add3_u32 v4, v56, v4, v58
	v_add3_u32 v5, v57, v5, v59
	v_add3_u32 v4, v60, v4, v62
	v_add3_u32 v5, v61, v5, v63
	s_branch .Lsc_p8b
.Lsc_p2b:
	s_cmp_eq_u32 s0, 0
	s_cbranch_scc1 .Lsc_pdb

.Lsc_pdb:
	s_and_b32 s0, s70, 0x7ffffffe
	s_cmp_lg_u32 s70, s0
	v_add_u32_e32 v4, v4, v5
	s_cselect_b64 s[38:39], -1, 0
	s_and_b64 vcc, exec, s[38:39]
	s_cbranch_vccnz .LBB0_1568
	s_branch .LBB0_1570
